# v041 + wave-wide fmax in the table-row quantization (ret_r1, LRU) and peer_v coefficient staging: 6 ds_bpermute round trips -> DPP butterfly + row_bcast + v_readlane
# speedup vs baseline: 1.0147x; 1.0055x over previous
; #define LAS __attribute__((address_space(3)))
; __device__ __forceinline__ f32x4 mfma16(bf16x8 a, bf16x8 b, f32x4 c) { return __builtin_amdgcn_mfma_f32_16x16x32_bf16(a, b, c, 0, 0, 0); }
; template <int ISV>
; __device__ __forceinline__ void quant_finish(const QRow& q, unsigned char* qtab, float* scales, int e, int lane) {
;     float amax = 0.f;
; #pragma unroll
;     for (int j = 0; j < 8; ++j) amax = fmaxf(amax, fmaxf(fmaxf(fabsf(q.v[j].x), fabsf(q.v[j].y)), fmaxf(fabsf(q.v[j].z), fabsf(q.v[j].w))));
;     amax = wave_max(amax);
;     unsigned* qp = (unsigned*)qtab + (size_t)e * 64;
;     {
;         const float inv = amax > 0.f ? 127.0f / amax : 0.f;
;         if (lane == 0) scales[e] = amax * (1.0f / 127.0f);
; __device__ __forceinline__ void ret_state_update(f32x4 (&S)[8], const LAS bf16_t* KT, const LAS bf16_t* VT, float dec, int wid, int fr, int fq) {
;     const unsigned lane = (unsigned)(fq * 16 + fr);
; #pragma unroll
;     for (int tt = 0; tt < 8; ++tt) S[tt] = S[tt] * dec;
; #pragma unroll
;     for (int ks = 0; ks < 2; ++ks) {
;         const bf16x8 bb = trb_frag((const LAS unsigned char*)VT, lane, wid, ks);
; #pragma unroll
;         for (int tt = 0; tt < 8; ++tt) { const bf16x8 a = trb_frag((const LAS unsigned char*)KT, lane, tt, ks); S[tt] = mfma16(a, bb, S[tt]); }
;     }
.LBB0_215:
	s_waitcnt lgkmcnt(0)
	s_barrier
	v_pk_mul_f32 v[160:161], v[190:191], v[164:165]
	v_pk_mul_f32 v[158:159], v[194:195], v[162:163]
	ds_read_b64_tr_b16 v[162:163], v217 offset:18432
	ds_read_b64_tr_b16 v[164:165], v218 offset:18688
	ds_read_b64_tr_b16 v[224:225], v219
	ds_read_b64_tr_b16 v[226:227], v220 offset:256
	v_pk_mul_f32 v[132:133], v[190:191], v[132:133]
	v_pk_mul_f32 v[130:131], v[194:195], v[130:131]
	v_pk_mul_f32 v[136:137], v[190:191], v[136:137]
	v_pk_mul_f32 v[134:135], v[194:195], v[134:135]
	s_waitcnt lgkmcnt(0)
	v_mfma_f32_16x16x32_bf16 v[130:133], v[224:227], v[162:165], v[130:133]
	ds_read_b64_tr_b16 v[224:225], v221
	ds_read_b64_tr_b16 v[226:227], v222 offset:256
	v_pk_mul_f32 v[140:141], v[190:191], v[140:141]
	v_pk_mul_f32 v[138:139], v[194:195], v[138:139]
	s_waitcnt lgkmcnt(0)
	v_mfma_f32_16x16x32_bf16 v[134:137], v[224:227], v[162:165], v[134:137]
	ds_read_b64_tr_b16 v[224:225], v219 offset:512
	ds_read_b64_tr_b16 v[226:227], v220 offset:768
	v_pk_mul_f32 v[144:145], v[190:191], v[144:145]
	v_pk_mul_f32 v[142:143], v[194:195], v[142:143]
	s_waitcnt lgkmcnt(0)
	v_mfma_f32_16x16x32_bf16 v[138:141], v[224:227], v[162:165], v[138:141]
	ds_read_b64_tr_b16 v[224:225], v221 offset:512
	ds_read_b64_tr_b16 v[226:227], v222 offset:768
	v_pk_mul_f32 v[148:149], v[190:191], v[148:149]
	v_pk_mul_f32 v[146:147], v[194:195], v[146:147]
	s_waitcnt lgkmcnt(0)
	v_mfma_f32_16x16x32_bf16 v[142:145], v[224:227], v[162:165], v[142:145]
	ds_read_b64_tr_b16 v[224:225], v219 offset:1024
	ds_read_b64_tr_b16 v[226:227], v220 offset:1280
	v_pk_mul_f32 v[152:153], v[190:191], v[152:153]
	v_pk_mul_f32 v[150:151], v[194:195], v[150:151]
	s_waitcnt lgkmcnt(0)
	v_mfma_f32_16x16x32_bf16 v[146:149], v[224:227], v[162:165], v[146:149]
	ds_read_b64_tr_b16 v[224:225], v221 offset:1024
	ds_read_b64_tr_b16 v[226:227], v222 offset:1280
	v_pk_mul_f32 v[156:157], v[190:191], v[156:157]
	v_pk_mul_f32 v[154:155], v[194:195], v[154:155]
	s_waitcnt lgkmcnt(0)
	v_mfma_f32_16x16x32_bf16 v[150:153], v[224:227], v[162:165], v[150:153]
	ds_read_b64_tr_b16 v[224:225], v219 offset:1536
	ds_read_b64_tr_b16 v[226:227], v220 offset:1792
	s_waitcnt lgkmcnt(0)
	v_mfma_f32_16x16x32_bf16 v[158:161], v[224:227], v[162:165], v[158:161]
	ds_read_b64_tr_b16 v[224:225], v221 offset:1536
	ds_read_b64_tr_b16 v[226:227], v222 offset:1792
	s_waitcnt lgkmcnt(0)
	v_mfma_f32_16x16x32_bf16 v[162:165], v[224:227], v[162:165], v[154:157]
	ds_read_b64_tr_b16 v[224:225], v217 offset:26624
	ds_read_b64_tr_b16 v[226:227], v218 offset:26880
	s_nop 0
	ds_read_b64_tr_b16 v[154:155], v219 offset:8192
	ds_read_b64_tr_b16 v[156:157], v220 offset:8448
	s_waitcnt lgkmcnt(0)
	v_mfma_f32_16x16x32_bf16 v[130:133], v[154:157], v[224:227], v[130:133]
	ds_read_b64_tr_b16 v[154:155], v221 offset:8192
	ds_read_b64_tr_b16 v[156:157], v222 offset:8448
	s_waitcnt lgkmcnt(0)
	v_mfma_f32_16x16x32_bf16 v[134:137], v[154:157], v[224:227], v[134:137]
	ds_read_b64_tr_b16 v[154:155], v219 offset:8704
	ds_read_b64_tr_b16 v[156:157], v220 offset:8960
	s_waitcnt lgkmcnt(0)
	v_mfma_f32_16x16x32_bf16 v[138:141], v[154:157], v[224:227], v[138:141]
	ds_read_b64_tr_b16 v[154:155], v221 offset:8704
	ds_read_b64_tr_b16 v[156:157], v222 offset:8960
	s_waitcnt lgkmcnt(0)
	v_mfma_f32_16x16x32_bf16 v[142:145], v[154:157], v[224:227], v[142:145]
	ds_read_b64_tr_b16 v[154:155], v219 offset:9216
	ds_read_b64_tr_b16 v[156:157], v220 offset:9472
	s_waitcnt lgkmcnt(0)
	v_mfma_f32_16x16x32_bf16 v[146:149], v[154:157], v[224:227], v[146:149]
	ds_read_b64_tr_b16 v[154:155], v221 offset:9216
	ds_read_b64_tr_b16 v[156:157], v222 offset:9472
	s_waitcnt lgkmcnt(0)
	v_mfma_f32_16x16x32_bf16 v[150:153], v[154:157], v[224:227], v[150:153]
	ds_read_b64_tr_b16 v[154:155], v219 offset:9728
	ds_read_b64_tr_b16 v[156:157], v220 offset:9984
	s_waitcnt lgkmcnt(0)
	v_mfma_f32_16x16x32_bf16 v[154:157], v[154:157], v[224:227], v[158:161]
	s_nop 2
	ds_read_b64_tr_b16 v[158:159], v221 offset:9728
	ds_read_b64_tr_b16 v[160:161], v222 offset:9984
	s_waitcnt lgkmcnt(0)
	v_mfma_f32_16x16x32_bf16 v[158:161], v[158:161], v[224:227], v[162:165]
	s_waitcnt vmcnt(15)
	s_nop 1
	v_max_f32_e64 v162, |v129|, |v129|
	v_max_f32_e64 v163, |v128|, |v128|
	v_max_f32_e32 v162, v163, v162
	s_waitcnt vmcnt(14)
	v_max_f32_e64 v163, |v125|, |v125|
	v_max_f32_e64 v164, |v124|, |v124|
	v_max_f32_e32 v163, v164, v163
	v_max3_f32 v162, |v126|, |v127|, v162
	v_max3_f32 v163, |v122|, |v123|, v163
	v_max3_f32 v162, v162, 0, v163
	s_waitcnt vmcnt(13)
	v_max_f32_e64 v163, |v121|, |v121|
	v_max_f32_e64 v164, |v120|, |v120|
	v_max_f32_e32 v163, v164, v163
	s_waitcnt vmcnt(12)
	v_max_f32_e64 v164, |v117|, |v117|
	v_max_f32_e64 v165, |v116|, |v116|
	v_max_f32_e32 v164, v165, v164
	v_max3_f32 v163, |v118|, |v119|, v163
	v_max3_f32 v164, |v114|, |v115|, v164
	v_max3_f32 v162, v162, v163, v164
	s_waitcnt vmcnt(11)
	v_max_f32_e64 v163, |v113|, |v113|
	v_max_f32_e64 v164, |v112|, |v112|
	v_max_f32_e32 v163, v164, v163
	s_waitcnt vmcnt(10)
	v_max_f32_e64 v164, |v109|, |v109|
	v_max_f32_e64 v165, |v108|, |v108|
	v_max_f32_e32 v164, v165, v164
	v_max3_f32 v163, |v110|, |v111|, v163
	v_max3_f32 v164, |v106|, |v107|, v164
	v_max3_f32 v162, v162, v163, v164
	s_waitcnt vmcnt(9)
	v_max_f32_e64 v163, |v105|, |v105|
	v_max_f32_e64 v164, |v104|, |v104|
	v_max_f32_e32 v163, v164, v163
	s_waitcnt vmcnt(8)
	v_max_f32_e64 v164, |v101|, |v101|
	v_max_f32_e64 v165, |v100|, |v100|
	v_max_f32_e32 v164, v165, v164
	v_max3_f32 v163, |v102|, |v103|, v163
	v_max3_f32 v164, |v98|, |v99|, v164
	v_max3_f32 v162, v162, v163, v164
	s_nop 1
	v_max_f32_dpp v162, v162, v162 quad_perm:[1,0,3,2] row_mask:0xf bank_mask:0xf
	s_nop 1
	v_max_f32_dpp v162, v162, v162 quad_perm:[2,3,0,1] row_mask:0xf bank_mask:0xf
	s_nop 1
	v_max_f32_dpp v162, v162, v162 row_half_mirror row_mask:0xf bank_mask:0xf
	s_nop 1
	v_max_f32_dpp v162, v162, v162 row_mirror row_mask:0xf bank_mask:0xf
	s_nop 1
	v_max_f32_dpp v162, v162, v162 row_bcast:15 row_mask:0xa bank_mask:0xf
	s_nop 1
	v_max_f32_dpp v162, v162, v162 row_bcast:31 row_mask:0xc bank_mask:0xf
	s_nop 1
	v_readlane_b32 s98, v162, 63
	s_nop 1
	v_mov_b32_e32 v162, s98
	v_max_f32_e32 v163, v162, v162
	s_and_saveexec_b64 s[6:7], s[38:39]
	s_cbranch_execz .LBB0_217
	s_lshl_b64 s[22:23], s[48:49], 2
	s_add_u32 s22, s50, s22
	s_addc_u32 s23, s51, s23
	v_mul_f32_e32 v163, 0x3c010204, v162
	global_store_dword v175, v163, s[22:23]

; __device__ __forceinline__ unsigned pk2(float lo, float hi) { const f32x2c_t v = {lo, hi}; const bf16x2c_t b = __builtin_convertvector(v, bf16x2c_t); return __builtin_bit_cast(unsigned, b); }
; __device__ __forceinline__ float bflo(unsigned w) { return __uint_as_float(w << 16); }
; __device__ __forceinline__ float bfhi(unsigned w) { return __uint_as_float(w & 0xffff0000u); }
; __device__ __forceinline__ float gelu_tanh(float x) { const float y = 0.7978845608028654f * (x + 0.044715f * x * x * x); return x * __builtin_amdgcn_rcpf(1.0f + fexp_(-2.0f * y)); }
; template <int MODE> ...
;     ...
;             float hcur = hin;
; #pragma unroll
;             for (int q = 0; q < 16; ++q) { const int o = (seg * 16 + q) * 132 + sj; const float a = AA[o]; hcur = a * hcur + BB[o]; acum *= a; BB[o] = hcur; AA[o] = acum; }
;             __syncthreads();
;             const unsigned gw[8] = {gc0.x, gc0.y, gc0.z, gc0.w, gc1.x, gc1.y, gc1.z, gc1.w};
;             unsigned oy[8], ow[8];
; #pragma unroll
;             for (int q = 0; q < 8; ++q) { const float g0 = gelu_tanh(bflo(gw[q])), g1 = gelu_tanh(bfhi(gw[q]));
;                 oy[q] = pk2(BB[m * 132 + j0 + 2 * q] * g0, BB[m * 132 + j0 + 2 * q + 1] * g1);
;                 ow[q] = pk2(AA[m * 132 + j0 + 2 * q] * g0, AA[m * 132 + j0 + 2 * q + 1] * g1); }
.LBB0_269:
	s_or_b64 exec, exec, s[6:7]
	v_fma_f32 v238, v50, v222, v238
	v_fmac_f32_e32 v239, v238, v223
	v_mul_f32_e32 v222, v51, v222
	v_mul_f32_e32 v223, v222, v223
	ds_write2_b32 v158, v238, v239 offset1:132
	ds_write2_b32 v66, v222, v223 offset1:132
	v_fma_f32 v240, v239, v224, v240
	v_fmac_f32_e32 v241, v240, v225
	v_mul_f32_e32 v224, v223, v224
	v_mul_f32_e32 v225, v224, v225
	ds_write2_b32 v65, v240, v241 offset0:8 offset1:140
	ds_write2_b32 v64, v224, v225 offset0:8 offset1:140
	v_fma_f32 v244, v241, v226, v244
	v_fmac_f32_e32 v245, v244, v227
	v_mul_f32_e32 v226, v225, v226
	v_mul_f32_e32 v227, v226, v227
	ds_write2_b32 v63, v244, v245 offset0:16 offset1:148
	ds_write2_b32 v62, v226, v227 offset0:16 offset1:148
	v_fma_f32 v246, v245, v228, v246
	v_fmac_f32_e32 v247, v246, v229
	v_mul_f32_e32 v228, v227, v228
	v_mul_f32_e32 v229, v228, v229
	ds_write2_b32 v61, v246, v247 offset0:24 offset1:156
	ds_write2_b32 v60, v228, v229 offset0:24 offset1:156
	v_fma_f32 v248, v247, v230, v248
	v_fmac_f32_e32 v249, v248, v231
	v_mul_f32_e32 v230, v229, v230
	v_mul_f32_e32 v231, v230, v231
	ds_write2_b32 v59, v248, v249 offset0:32 offset1:164
	ds_write2_b32 v58, v230, v231 offset0:32 offset1:164
	v_fma_f32 v250, v249, v232, v250
	v_fmac_f32_e32 v251, v250, v233
	v_mul_f32_e32 v232, v231, v232
	v_mul_f32_e32 v233, v232, v233
	ds_write2_b32 v57, v250, v251 offset0:40 offset1:172
	ds_write2_b32 v56, v232, v233 offset0:40 offset1:172
	v_fma_f32 v252, v251, v234, v252
	v_fmac_f32_e32 v253, v252, v235
	v_mul_f32_e32 v234, v233, v234
	v_mul_f32_e32 v235, v234, v235
	ds_write2_b32 v55, v252, v253 offset0:48 offset1:180
	ds_write2_b32 v54, v234, v235 offset0:48 offset1:180
	v_fma_f32 v254, v253, v236, v254
	v_fmac_f32_e32 v255, v254, v237
	v_mul_f32_e32 v236, v235, v236
	v_mul_f32_e32 v237, v236, v237
	ds_write2_b32 v53, v254, v255 offset0:56 offset1:188
	ds_write2_b32 v52, v236, v237 offset0:56 offset1:188
	s_waitcnt lgkmcnt(0)
	s_barrier
	s_mov_b32 s100, 0xbdd2d3e7
	s_mov_b32 s101, 0xc0135761
	ds_read_b128 v[50:53], v164
	ds_read_b128 v[222:225], v164 offset:51200
	ds_read_b128 v[54:57], v164 offset:16
	ds_read_b128 v[226:229], v164 offset:51216
	ds_read_b128 v[58:61], v164 offset:32
	ds_read_b128 v[230:233], v164 offset:51232
	ds_read_b128 v[62:65], v164 offset:48
	ds_read_b128 v[234:237], v164 offset:51248
	v_lshlrev_b32_e32 v238, 16, v6
	v_lshlrev_b32_e32 v240, 16, v7
	v_and_b32_e32 v239, 0xffff0000, v6
	v_and_b32_e32 v241, 0xffff0000, v7
	v_pk_mul_f32 v[66:67], v[238:239], v[238:239]
	v_pk_mul_f32 v[68:69], v[240:241], v[240:241]
	v_pk_fma_f32 v[66:67], v[66:67], s[100:101], s[100:101] op_sel:[0,0,1] op_sel_hi:[1,0,1]
	v_pk_fma_f32 v[68:69], v[68:69], s[100:101], s[100:101] op_sel:[0,0,1] op_sel_hi:[1,0,1]
	v_pk_mul_f32 v[66:67], v[66:67], v[238:239]
	v_pk_mul_f32 v[68:69], v[68:69], v[240:241]
	v_exp_f32_e32 v66, v66
	v_exp_f32_e32 v67, v67
	v_exp_f32_e32 v68, v68
	v_exp_f32_e32 v69, v69
	v_pk_add_f32 v[66:67], v[66:67], 1.0 op_sel_hi:[1,0]
	v_pk_add_f32 v[68:69], v[68:69], 1.0 op_sel_hi:[1,0]
	v_rcp_f32_e32 v66, v66
	v_rcp_f32_e32 v67, v67
	v_rcp_f32_e32 v68, v68
	v_rcp_f32_e32 v69, v69
	v_pk_mul_f32 v[238:239], v[66:67], v[238:239]
	v_pk_mul_f32 v[240:241], v[68:69], v[240:241]
	v_lshlrev_b32_e32 v244, 16, v8
	v_lshlrev_b32_e32 v246, 16, v9
	v_and_b32_e32 v245, 0xffff0000, v8
	v_and_b32_e32 v247, 0xffff0000, v9
	v_pk_mul_f32 v[66:67], v[244:245], v[244:245]
	v_pk_mul_f32 v[68:69], v[246:247], v[246:247]
	v_pk_fma_f32 v[66:67], v[66:67], s[100:101], s[100:101] op_sel:[0,0,1] op_sel_hi:[1,0,1]
	v_pk_fma_f32 v[68:69], v[68:69], s[100:101], s[100:101] op_sel:[0,0,1] op_sel_hi:[1,0,1]
	v_pk_mul_f32 v[66:67], v[66:67], v[244:245]
	v_pk_mul_f32 v[68:69], v[68:69], v[246:247]
	v_exp_f32_e32 v66, v66
	v_exp_f32_e32 v67, v67
	v_exp_f32_e32 v68, v68
	v_exp_f32_e32 v69, v69
	v_pk_add_f32 v[66:67], v[66:67], 1.0 op_sel_hi:[1,0]
	v_pk_add_f32 v[68:69], v[68:69], 1.0 op_sel_hi:[1,0]
	v_rcp_f32_e32 v66, v66
	v_rcp_f32_e32 v67, v67
	v_rcp_f32_e32 v68, v68
	v_rcp_f32_e32 v69, v69
	v_pk_mul_f32 v[244:245], v[66:67], v[244:245]
	v_pk_mul_f32 v[246:247], v[68:69], v[246:247]
	v_lshlrev_b32_e32 v248, 16, v2
	v_lshlrev_b32_e32 v250, 16, v3
	v_and_b32_e32 v249, 0xffff0000, v2
	v_and_b32_e32 v251, 0xffff0000, v3
	v_pk_mul_f32 v[66:67], v[248:249], v[248:249]
	v_pk_mul_f32 v[68:69], v[250:251], v[250:251]
	v_pk_fma_f32 v[66:67], v[66:67], s[100:101], s[100:101] op_sel:[0,0,1] op_sel_hi:[1,0,1]
	v_pk_fma_f32 v[68:69], v[68:69], s[100:101], s[100:101] op_sel:[0,0,1] op_sel_hi:[1,0,1]
	v_pk_mul_f32 v[66:67], v[66:67], v[248:249]
	v_pk_mul_f32 v[68:69], v[68:69], v[250:251]
	v_exp_f32_e32 v66, v66
	v_exp_f32_e32 v67, v67
	v_exp_f32_e32 v68, v68
	v_exp_f32_e32 v69, v69
	v_pk_add_f32 v[66:67], v[66:67], 1.0 op_sel_hi:[1,0]
	v_pk_add_f32 v[68:69], v[68:69], 1.0 op_sel_hi:[1,0]
	v_rcp_f32_e32 v66, v66
	v_rcp_f32_e32 v67, v67
	v_rcp_f32_e32 v68, v68
	v_rcp_f32_e32 v69, v69
	v_pk_mul_f32 v[248:249], v[66:67], v[248:249]
	v_pk_mul_f32 v[250:251], v[68:69], v[250:251]
	v_lshlrev_b32_e32 v252, 16, v4
	v_lshlrev_b32_e32 v254, 16, v5
	v_and_b32_e32 v253, 0xffff0000, v4
	v_and_b32_e32 v255, 0xffff0000, v5
	v_pk_mul_f32 v[66:67], v[252:253], v[252:253]
	v_pk_mul_f32 v[68:69], v[254:255], v[254:255]
	v_pk_fma_f32 v[66:67], v[66:67], s[100:101], s[100:101] op_sel:[0,0,1] op_sel_hi:[1,0,1]
	v_pk_fma_f32 v[68:69], v[68:69], s[100:101], s[100:101] op_sel:[0,0,1] op_sel_hi:[1,0,1]
	v_pk_mul_f32 v[66:67], v[66:67], v[252:253]
	v_pk_mul_f32 v[68:69], v[68:69], v[254:255]
	v_exp_f32_e32 v66, v66
	v_exp_f32_e32 v67, v67
	v_exp_f32_e32 v68, v68
	v_exp_f32_e32 v69, v69
	v_pk_add_f32 v[66:67], v[66:67], 1.0 op_sel_hi:[1,0]
	v_pk_add_f32 v[68:69], v[68:69], 1.0 op_sel_hi:[1,0]
	v_rcp_f32_e32 v66, v66
	v_rcp_f32_e32 v67, v67
	v_rcp_f32_e32 v68, v68
	v_rcp_f32_e32 v69, v69
	v_pk_mul_f32 v[252:253], v[66:67], v[252:253]
	v_pk_mul_f32 v[254:255], v[68:69], v[254:255]
	s_waitcnt lgkmcnt(0)
; __device__ __forceinline__ unsigned pk2(float lo, float hi) { const f32x2c_t v = {lo, hi}; const bf16x2c_t b = __builtin_convertvector(v, bf16x2c_t); return __builtin_bit_cast(unsigned, b); }
; __device__ __forceinline__ float bflo(unsigned w) { return __uint_as_float(w << 16); }
; __device__ __forceinline__ float bfhi(unsigned w) { return __uint_as_float(w & 0xffff0000u); }
; __device__ __forceinline__ float gelu_tanh(float x) { const float y = 0.7978845608028654f * (x + 0.044715f * x * x * x); return x * __builtin_amdgcn_rcpf(1.0f + fexp_(-2.0f * y)); }
; template <int ISV>
; __device__ __forceinline__ void quant_finish(const QRow& q, unsigned char* qtab, float* scales, int e, int lane) {
;     float amax = 0.f;
; #pragma unroll
;     for (int j = 0; j < 8; ++j) amax = fmaxf(amax, fmaxf(fmaxf(fabsf(q.v[j].x), fabsf(q.v[j].y)), fmaxf(fabsf(q.v[j].z), fabsf(q.v[j].w))));
;     amax = wave_max(amax);
;     unsigned* qp = (unsigned*)qtab + (size_t)e * 64;
;     {
;         const float inv = amax > 0.f ? 127.0f / amax : 0.f;
;         if (lane == 0) scales[e] = amax * (1.0f / 127.0f);
; template <int MODE> ...
;     ...
;             for (int q = 0; q < 8; ++q) { const float g0 = gelu_tanh(bflo(gw[q])), g1 = gelu_tanh(bfhi(gw[q]));
;                 oy[q] = pk2(BB[m * 132 + j0 + 2 * q] * g0, BB[m * 132 + j0 + 2 * q + 1] * g1);
;                 ow[q] = pk2(AA[m * 132 + j0 + 2 * q] * g0, AA[m * 132 + j0 + 2 * q + 1] * g1); }
;             const size_t yo = (size_t)(n * 64 + m) * 1024 + c0 + j0;
;             *(u32x4*)(Y0 + yo) = (u32x4){oy[0], oy[1], oy[2], oy[3]}; *(u32x4*)(Y0 + yo + 8) = (u32x4){oy[4], oy[5], oy[6], oy[7]};
;             *(u32x4*)(W0 + yo) = (u32x4){ow[0], ow[1], ow[2], ow[3]}; *(u32x4*)(W0 + yo + 8) = (u32x4){ow[4], ow[5], ow[6], ow[7]};
	v_pk_mul_f32 v[66:67], v[238:239], v[50:51]
	v_pk_mul_f32 v[238:239], v[238:239], v[222:223]
	v_cvt_pk_bf16_f32 v50, v66, v67
	v_cvt_pk_bf16_f32 v6, v238, v239
	v_pk_mul_f32 v[68:69], v[240:241], v[52:53]
	v_pk_mul_f32 v[240:241], v[240:241], v[224:225]
	v_cvt_pk_bf16_f32 v51, v68, v69
	v_cvt_pk_bf16_f32 v7, v240, v241
	v_pk_mul_f32 v[66:67], v[244:245], v[54:55]
	v_pk_mul_f32 v[244:245], v[244:245], v[226:227]
	v_cvt_pk_bf16_f32 v52, v66, v67
	v_cvt_pk_bf16_f32 v8, v244, v245
	v_pk_mul_f32 v[68:69], v[246:247], v[56:57]
	v_pk_mul_f32 v[246:247], v[246:247], v[228:229]
	v_cvt_pk_bf16_f32 v53, v68, v69
	v_cvt_pk_bf16_f32 v9, v246, v247
	v_pk_mul_f32 v[66:67], v[248:249], v[58:59]
	v_pk_mul_f32 v[248:249], v[248:249], v[230:231]
	v_cvt_pk_bf16_f32 v54, v66, v67
	v_cvt_pk_bf16_f32 v2, v248, v249
	v_pk_mul_f32 v[68:69], v[250:251], v[60:61]
	v_pk_mul_f32 v[250:251], v[250:251], v[232:233]
	v_cvt_pk_bf16_f32 v55, v68, v69
	v_cvt_pk_bf16_f32 v3, v250, v251
	v_pk_mul_f32 v[66:67], v[252:253], v[62:63]
	v_pk_mul_f32 v[252:253], v[252:253], v[234:235]
	v_cvt_pk_bf16_f32 v56, v66, v67
	v_cvt_pk_bf16_f32 v4, v252, v253
	v_pk_mul_f32 v[68:69], v[254:255], v[64:65]
	v_pk_mul_f32 v[254:255], v[254:255], v[236:237]
	v_cvt_pk_bf16_f32 v57, v68, v69
	v_cvt_pk_bf16_f32 v5, v254, v255
	v_lshl_add_u32 v58, s0, 6, v79
	v_ashrrev_i32_e32 v59, 31, v58
	v_lshlrev_b64 v[58:59], 10, v[58:59]
	v_or_b32_e32 v58, s18, v58
	v_or_b32_e32 v58, v58, v78
	v_lshlrev_b64 v[58:59], 1, v[58:59]
	v_lshl_add_u64 v[60:61], s[72:73], 0, v[58:59]
	v_lshl_add_u64 v[62:63], s[90:91], 0, v[58:59]
	global_store_dwordx4 v[60:61], v[50:53], off
	global_store_dwordx4 v[60:61], v[54:57], off offset:16
	global_store_dwordx4 v[62:63], v[6:9], off
	global_store_dwordx4 v[62:63], v[2:5], off offset:16
	s_waitcnt vmcnt(11)
	s_nop 0
	v_max_f32_e64 v2, |v49|, |v49|
	v_max_f32_e64 v3, |v48|, |v48|
	v_max_f32_e32 v2, v3, v2
	s_waitcnt vmcnt(10)
	v_max_f32_e64 v3, |v45|, |v45|
	v_max_f32_e64 v4, |v44|, |v44|
	v_max_f32_e32 v3, v4, v3
	v_max3_f32 v2, |v46|, |v47|, v2
	v_max3_f32 v3, |v42|, |v43|, v3
	v_max3_f32 v2, v2, 0, v3
	s_waitcnt vmcnt(9)
	v_max_f32_e64 v3, |v41|, |v41|
	v_max_f32_e64 v4, |v40|, |v40|
	v_max_f32_e32 v3, v4, v3
	s_waitcnt vmcnt(8)
	v_max_f32_e64 v4, |v37|, |v37|
	v_max_f32_e64 v5, |v36|, |v36|
	v_max_f32_e32 v4, v5, v4
	v_max3_f32 v3, |v38|, |v39|, v3
	v_max3_f32 v4, |v34|, |v35|, v4
	v_max3_f32 v2, v2, v3, v4
	s_waitcnt vmcnt(7)
	v_max_f32_e64 v3, |v33|, |v33|
	v_max_f32_e64 v4, |v32|, |v32|
	v_max_f32_e32 v3, v4, v3
	s_waitcnt vmcnt(6)
	v_max_f32_e64 v4, |v29|, |v29|
	v_max_f32_e64 v5, |v28|, |v28|
	v_max_f32_e32 v4, v5, v4
	v_max3_f32 v3, |v30|, |v31|, v3
	v_max3_f32 v4, |v26|, |v27|, v4
	v_max3_f32 v2, v2, v3, v4
	s_waitcnt vmcnt(5)
	v_max_f32_e64 v3, |v25|, |v25|
	v_max_f32_e64 v4, |v24|, |v24|
	v_max_f32_e32 v3, v4, v3
	s_waitcnt vmcnt(4)
	v_max_f32_e64 v4, |v21|, |v21|
	v_max_f32_e64 v5, |v20|, |v20|
	v_max_f32_e32 v4, v5, v4
	v_max3_f32 v3, |v22|, |v23|, v3
	v_max3_f32 v4, |v18|, |v19|, v4
	v_max3_f32 v2, v2, v3, v4
	s_nop 1
	v_max_f32_dpp v2, v2, v2 quad_perm:[1,0,3,2] row_mask:0xf bank_mask:0xf
	s_nop 1
	v_max_f32_dpp v2, v2, v2 quad_perm:[2,3,0,1] row_mask:0xf bank_mask:0xf
	s_nop 1
	v_max_f32_dpp v2, v2, v2 row_half_mirror row_mask:0xf bank_mask:0xf
	s_nop 1
	v_max_f32_dpp v2, v2, v2 row_mirror row_mask:0xf bank_mask:0xf
	s_nop 1
	v_max_f32_dpp v2, v2, v2 row_bcast:15 row_mask:0xa bank_mask:0xf
	s_nop 1
	v_max_f32_dpp v2, v2, v2 row_bcast:31 row_mask:0xc bank_mask:0xf
	s_nop 1
	v_readlane_b32 s98, v2, 63
	s_nop 1
	v_mov_b32_e32 v2, s98
	v_max_f32_e32 v3, v2, v2
	s_and_saveexec_b64 s[6:7], s[40:41]
	s_cbranch_execz .LBB0_240
	s_lshl_b64 s[22:23], s[48:49], 2
	s_add_u32 s22, s86, s22
	s_addc_u32 s23, s87, s23
	v_mul_f32_e32 v3, 0x3c010204, v2
	global_store_dword v85, v3, s[22:23]
	s_branch .LBB0_240

; #define LAS __attribute__((address_space(3)))
; __device__ __forceinline__ void peer_stage_lists(const PeerMeta& m, LAS int* es, LAS unsigned* crep, LAS float* scp, int lane) {
;     es[lane] = m.e[0] << 8; es[64 + lane] = m.e[1] << 8;
;     const float cmax = wave_max(fmaxf(fabsf(m.c[0]), fabsf(m.c[1])));
;     const float inv = cmax > 0.f ? 127.0f / cmax : 0.f;
;     if (lane == 0) scp[0] = cmax * (1.0f / 127.0f);
; #pragma unroll
;     for (int hh = 0; hh < 2; ++hh) {
;         const int h = (int)rintf(m.c[hh] * inv);
;         crep[hh * 64 + (lane & 3) * 16 + (lane >> 2)] = (unsigned)(h & 255) * 0x01010101u;
;     }
; }
; template <int STRIP>
; __device__ __forceinline__ void peer_v_phase(LAS unsigned char* lds, const unsigned char* VQs, const int* sel_e, const float* coef,
;                                              bf16_t* zs, int xi, int nx, int rank, int nloc) {
;     ...
;             peer_meta_load(m0, sel_e, coef, wx, lane);
;             peer_stage_lists(m0, esb, (LAS unsigned*)(wl + 1024), (LAS float*)(wl + 2048), lane);
;             asm volatile("" ::: "memory");
;             peer_meta_load(m0, sel_e, coef, wx + min(1, NT - 1) * nwx, lane);
;             peer_meta_load(m1, sel_e, coef, wx + min(2, NT - 1) * nwx, lane);
;             asm volatile("" ::: "memory");
; #pragma unroll
;             for (int it = 0; it < 16; ++it) A[it] = *(const u32x4*)(Vj + ((unsigned)esb[4 * it + r] + li));
;             asm volatile("" ::: "memory");
; #pragma unroll
;             for (int it = 0; it < 16; ++it) B[it] = *(const u32x4*)(Vj + ((unsigned)esb[64 + 4 * it + r] + li));
;             asm volatile("" ::: "memory");
.LBB0_941:
	global_load_dword v4, v[130:131], off
	global_load_dword v5, v[130:131], off offset:256
	global_load_dword v2, v[132:133], off
	global_load_dword v3, v[132:133], off offset:256
	s_waitcnt vmcnt(3)
	v_lshlrev_b32_e32 v4, 8, v4
	s_waitcnt vmcnt(2)
	v_lshlrev_b32_e32 v5, 8, v5
	ds_write2st64_b32 v154, v4, v5 offset1:1
	s_waitcnt vmcnt(0)
	v_max_f32_e64 v4, |v3|, |v3|
	v_max_f32_e64 v5, |v2|, |v2|
	v_max_f32_e32 v4, v5, v4
	s_nop 1
	v_max_f32_dpp v4, v4, v4 quad_perm:[1,0,3,2] row_mask:0xf bank_mask:0xf
	s_nop 1
	v_max_f32_dpp v4, v4, v4 quad_perm:[2,3,0,1] row_mask:0xf bank_mask:0xf
	s_nop 1
	v_max_f32_dpp v4, v4, v4 row_half_mirror row_mask:0xf bank_mask:0xf
	s_nop 1
	v_max_f32_dpp v4, v4, v4 row_mirror row_mask:0xf bank_mask:0xf
	s_nop 1
	v_max_f32_dpp v4, v4, v4 row_bcast:15 row_mask:0xa bank_mask:0xf
	s_nop 1
	v_max_f32_dpp v4, v4, v4 row_bcast:31 row_mask:0xc bank_mask:0xf
	s_nop 1
	v_readlane_b32 s98, v4, 63
	s_nop 1
	v_mov_b32_e32 v4, s98
	v_max_f32_e32 v5, v4, v4
	s_and_saveexec_b64 s[6:7], s[2:3]
	v_mul_f32_e32 v5, 0x3c010204, v4
	v_mov_b32_e32 v6, s11
	ds_write_b32 v6, v5 offset:2048
	s_or_b64 exec, exec, s[6:7]
	v_div_scale_f32 v5, s[6:7], v4, v4, s12
	v_rcp_f32_e32 v6, v5
	v_div_scale_f32 v7, vcc, s12, v4, s12
	s_ashr_i32 s37, s36, 31
	v_fma_f32 v8, -v5, v6, 1.0
	v_fmac_f32_e32 v6, v8, v6
	v_mul_f32_e32 v8, v7, v6
	v_fma_f32 v9, -v5, v8, v7
	v_fmac_f32_e32 v8, v9, v6
	v_fma_f32 v5, -v5, v8, v7
	v_div_fmas_f32 v5, v5, v6, v8
	v_div_fixup_f32 v5, v5, v4, s12
	v_cmp_lt_f32_e32 vcc, 0, v4
	s_lshl_b64 s[6:7], s[36:37], 22
	s_add_u32 s38, s9, s6
	v_cndmask_b32_e32 v4, 0, v5, vcc
	v_mul_f32_e32 v2, v2, v4
	v_mul_f32_e32 v3, v3, v4
	v_rndne_f32_e32 v2, v2
	v_rndne_f32_e32 v3, v3
	v_cvt_i32_f32_e32 v2, v2
	v_cvt_i32_f32_e32 v3, v3
	s_addc_u32 s39, s10, s7
	s_andn2_b64 vcc, exec, s[4:5]
	v_and_b32_e32 v2, 0xff, v2
	v_and_b32_e32 v3, 0xff, v3
	v_mul_lo_u32 v2, v2, s13
	v_mul_lo_u32 v3, v3, s13
	ds_write2st64_b32 v161, v2, v3 offset0:4 offset1:5
	global_load_dword v171, v[134:135], off
	global_load_dword v172, v[134:135], off offset:256
	global_load_dword v166, v[136:137], off
	global_load_dword v165, v[136:137], off offset:256
	global_load_dword v169, v[138:139], off
	global_load_dword v170, v[138:139], off offset:256
	global_load_dword v168, v[140:141], off
	global_load_dword v167, v[140:141], off offset:256
	ds_read2_b32 v[2:3], v162 offset1:4
	ds_read2_b32 v[4:5], v162 offset0:8 offset1:12
	s_waitcnt lgkmcnt(1)
	v_add_u32_e32 v2, v2, v153
	v_add_u32_e32 v3, v3, v153
	global_load_dwordx4 v[82:85], v2, s[38:39]
	global_load_dwordx4 v[74:77], v3, s[38:39]
	s_waitcnt lgkmcnt(0)
	v_add_u32_e32 v4, v4, v153
	ds_read2_b32 v[2:3], v162 offset0:16 offset1:20
	v_add_u32_e32 v5, v5, v153
	global_load_dwordx4 v[98:101], v4, s[38:39]
	global_load_dwordx4 v[38:41], v5, s[38:39]
	ds_read2_b32 v[4:5], v162 offset0:24 offset1:28
	s_waitcnt lgkmcnt(1)
	v_add_u32_e32 v2, v2, v153
	v_add_u32_e32 v3, v3, v153
	global_load_dwordx4 v[50:53], v2, s[38:39]
	global_load_dwordx4 v[34:37], v3, s[38:39]
	s_waitcnt lgkmcnt(0)
	v_add_u32_e32 v4, v4, v153
	ds_read2_b32 v[2:3], v162 offset0:32 offset1:36
	v_add_u32_e32 v5, v5, v153
	global_load_dwordx4 v[54:57], v4, s[38:39]
	global_load_dwordx4 v[26:29], v5, s[38:39]
	ds_read2_b32 v[4:5], v162 offset0:40 offset1:44
	s_waitcnt lgkmcnt(1)
	v_add_u32_e32 v2, v2, v153
	v_add_u32_e32 v3, v3, v153
	global_load_dwordx4 v[46:49], v2, s[38:39]
	global_load_dwordx4 v[30:33], v3, s[38:39]
	s_waitcnt lgkmcnt(0)
	v_add_u32_e32 v4, v4, v153
	ds_read2_b32 v[2:3], v162 offset0:48 offset1:52
	v_add_u32_e32 v5, v5, v153
	global_load_dwordx4 v[22:25], v4, s[38:39]
	global_load_dwordx4 v[14:17], v5, s[38:39]
	ds_read2_b32 v[4:5], v162 offset0:56 offset1:60
	s_waitcnt lgkmcnt(1)
	v_add_u32_e32 v2, v2, v153
	v_add_u32_e32 v3, v3, v153
	global_load_dwordx4 v[18:21], v2, s[38:39]
	global_load_dwordx4 v[10:13], v3, s[38:39]
	s_waitcnt lgkmcnt(0)
	v_add_u32_e32 v2, v4, v153
	v_add_u32_e32 v3, v5, v153
	global_load_dwordx4 v[6:9], v2, s[38:39]
	s_nop 0
	global_load_dwordx4 v[2:5], v3, s[38:39]
	ds_read2_b32 v[42:43], v162 offset0:64 offset1:68
	ds_read2_b32 v[44:45], v162 offset0:72 offset1:76
	s_waitcnt lgkmcnt(1)
	v_add_u32_e32 v42, v42, v153
	v_add_u32_e32 v43, v43, v153
	global_load_dwordx4 v[122:125], v42, s[38:39]
	global_load_dwordx4 v[118:121], v43, s[38:39]
	s_waitcnt lgkmcnt(0)
	v_add_u32_e32 v44, v44, v153
	ds_read2_b32 v[42:43], v162 offset0:80 offset1:84
	v_add_u32_e32 v45, v45, v153
	global_load_dwordx4 v[126:129], v44, s[38:39]
	global_load_dwordx4 v[90:93], v45, s[38:39]
	ds_read2_b32 v[44:45], v162 offset0:88 offset1:92
	s_waitcnt lgkmcnt(1)
	v_add_u32_e32 v42, v42, v153
	v_add_u32_e32 v43, v43, v153
	global_load_dwordx4 v[106:109], v42, s[38:39]
	global_load_dwordx4 v[86:89], v43, s[38:39]
	s_waitcnt lgkmcnt(0)
	v_add_u32_e32 v44, v44, v153
	ds_read2_b32 v[42:43], v162 offset0:96 offset1:100
	v_add_u32_e32 v45, v45, v153
	global_load_dwordx4 v[110:113], v44, s[38:39]
	global_load_dwordx4 v[78:81], v45, s[38:39]
	ds_read2_b32 v[44:45], v162 offset0:104 offset1:108
	s_waitcnt lgkmcnt(1)
	v_add_u32_e32 v42, v42, v153
	v_add_u32_e32 v43, v43, v153
	global_load_dwordx4 v[102:105], v42, s[38:39]
	global_load_dwordx4 v[94:97], v43, s[38:39]
	s_waitcnt lgkmcnt(0)
	v_add_u32_e32 v44, v44, v153
	ds_read2_b32 v[42:43], v162 offset0:112 offset1:116
	v_add_u32_e32 v45, v45, v153
	global_load_dwordx4 v[114:117], v44, s[38:39]
	global_load_dwordx4 v[66:69], v45, s[38:39]
	ds_read2_b32 v[44:45], v162 offset0:120 offset1:124
	s_waitcnt lgkmcnt(1)
	v_add_u32_e32 v42, v42, v153
	v_add_u32_e32 v43, v43, v153
	global_load_dwordx4 v[70:73], v42, s[38:39]
	global_load_dwordx4 v[62:65], v43, s[38:39]
	s_waitcnt lgkmcnt(0)
	v_add_u32_e32 v42, v44, v153
	v_add_u32_e32 v43, v45, v153
	global_load_dwordx4 v[58:61], v42, s[38:39]
	s_nop 0
	global_load_dwordx4 v[42:45], v43, s[38:39]
	s_cbranch_vccnz .LBB0_940
	s_lshl_b32 s6, s36, 8
	s_ashr_i32 s7, s6, 31
	v_lshl_add_u64 v[148:149], s[6:7], 1, v[146:147]
	s_mov_b32 s14, 0
	s_mov_b32 s40, s0
	s_branch .LBB0_946

; #define LAS __attribute__((address_space(3)))
; __device__ __forceinline__ void peer_stage_lists(const PeerMeta& m, LAS int* es, LAS unsigned* crep, LAS float* scp, int lane) {
;     es[lane] = m.e[0] << 8; es[64 + lane] = m.e[1] << 8;
;     const float cmax = wave_max(fmaxf(fabsf(m.c[0]), fabsf(m.c[1])));
;     const float inv = cmax > 0.f ? 127.0f / cmax : 0.f;
;     if (lane == 0) scp[0] = cmax * (1.0f / 127.0f);
; #pragma unroll
;     for (int hh = 0; hh < 2; ++hh) {
;         const int h = (int)rintf(m.c[hh] * inv);
;         crep[hh * 64 + (lane & 3) * 16 + (lane >> 2)] = (unsigned)(h & 255) * 0x01010101u;
;     }
; }
; __device__ __forceinline__ void acc_half_sel(i32x4 (&av)[4], const u32x4 (&R)[16], const LAS unsigned* cr  , int r, const unsigned (&mk)[4]) {
;     u32x4 c4[4];
; #pragma unroll
;     for (int q = 0; q < 4; ++q) c4[q] = *(const LAS u32x4*)(cr + r * 16 + 4 * q);
; #pragma unroll
;     for (int it = 0; it < 16; ++it) {
;         const unsigned rep = (it & 3) == 0 ? c4[it >> 2].x : (it & 3) == 1 ? c4[it >> 2].y : (it & 3) == 2 ? c4[it >> 2].z : c4[it >> 2].w;
;         i32x4 Aop; Aop.x = (int)(rep & mk[0]); Aop.y = (int)(rep & mk[1]); Aop.z = (int)(rep & mk[2]); Aop.w = (int)(rep & mk[3]);
;         av[it & 3] = __builtin_amdgcn_mfma_i32_16x16x64_i8(Aop, __builtin_bit_cast(i32x4, R[it]), av[it & 3], 0, 0, 0);
;     }
; }
.LBB0_946:
	s_waitcnt vmcnt(39)
	v_lshlrev_b32_e32 v171, 8, v171
	s_waitcnt vmcnt(38)
	v_lshlrev_b32_e32 v172, 8, v172
	ds_write2st64_b32 v154, v171, v172 offset0:2 offset1:3
	s_waitcnt vmcnt(36)
	v_max_f32_e64 v171, |v165|, |v165|
	v_max_f32_e64 v172, |v166|, |v166|
	v_max_f32_e32 v171, v172, v171
	s_nop 1
	v_max_f32_dpp v171, v171, v171 quad_perm:[1,0,3,2] row_mask:0xf bank_mask:0xf
	s_nop 1
	v_max_f32_dpp v171, v171, v171 quad_perm:[2,3,0,1] row_mask:0xf bank_mask:0xf
	s_nop 1
	v_max_f32_dpp v171, v171, v171 row_half_mirror row_mask:0xf bank_mask:0xf
	s_nop 1
	v_max_f32_dpp v171, v171, v171 row_mirror row_mask:0xf bank_mask:0xf
	s_nop 1
	v_max_f32_dpp v171, v171, v171 row_bcast:15 row_mask:0xa bank_mask:0xf
	s_nop 1
	v_max_f32_dpp v171, v171, v171 row_bcast:31 row_mask:0xc bank_mask:0xf
	s_nop 1
	v_readlane_b32 s98, v171, 63
	s_nop 1
	v_mov_b32_e32 v171, s98
	v_max_f32_e32 v172, v171, v171
	s_and_saveexec_b64 s[6:7], s[2:3]
	v_mul_f32_e32 v172, 0x3c010204, v171
	v_mov_b32_e32 v173, s11
	ds_write_b32 v173, v172 offset:2052
	s_or_b64 exec, exec, s[6:7]
	v_div_scale_f32 v172, s[6:7], v171, v171, s12
	v_rcp_f32_e32 v173, v172
	v_div_scale_f32 v174, vcc, s12, v171, s12
	s_add_i32 s6, s14, 3
	v_fma_f32 v175, -v172, v173, 1.0
	v_fmac_f32_e32 v173, v175, v173
	v_mul_f32_e32 v175, v174, v173
	v_fma_f32 v176, -v172, v175, v174
	v_fmac_f32_e32 v175, v176, v173
	v_fma_f32 v172, -v172, v175, v174
	v_div_fmas_f32 v172, v172, v173, v175
	v_div_fixup_f32 v172, v172, v171, s12
	v_cmp_lt_f32_e32 vcc, 0, v171
	s_min_i32 s6, s6, s1
	s_mul_i32 s6, s6, s54
	v_cndmask_b32_e32 v171, 0, v172, vcc
	v_mul_f32_e32 v166, v166, v171
	v_mul_f32_e32 v165, v165, v171
	v_rndne_f32_e32 v166, v166
	v_rndne_f32_e32 v165, v165
	v_cvt_i32_f32_e32 v166, v166
	v_cvt_i32_f32_e32 v165, v165
	s_add_i32 s6, s6, s0
	s_ashr_i32 s7, s6, 31
	v_and_b32_e32 v166, 0xff, v166
	v_and_b32_e32 v165, 0xff, v165
	v_mul_lo_u32 v166, v166, s13
	v_mul_lo_u32 v165, v165, s13
	ds_write2st64_b32 v161, v166, v165 offset0:6 offset1:7
	ds_read_b128 v[172:175], v163 offset:1024
	s_lshl_b64 s[6:7], s[6:7], 9
	s_ashr_i32 s41, s40, 31
	s_waitcnt vmcnt(35)
	v_lshlrev_b32_e32 v169, 8, v169
	s_waitcnt vmcnt(34)
	v_lshlrev_b32_e32 v170, 8, v170
	s_waitcnt lgkmcnt(0)
	v_and_b32_e32 v176, v172, v1
	v_and_b32_e32 v177, v172, v150
	v_and_b32_e32 v178, v172, v151
	v_and_b32_e32 v179, v172, v152
	v_and_b32_e32 v180, v173, v1
	v_and_b32_e32 v181, v173, v150
	s_waitcnt vmcnt(31)
	v_mfma_i32_16x16x64_i8 v[82:85], v[176:179], v[82:85], 0
	v_and_b32_e32 v176, v174, v1
	v_and_b32_e32 v177, v174, v150
	v_and_b32_e32 v178, v174, v151
	v_and_b32_e32 v179, v174, v152
	v_and_b32_e32 v182, v173, v151
	v_and_b32_e32 v183, v173, v152
	s_waitcnt vmcnt(29)
	v_mfma_i32_16x16x64_i8 v[98:101], v[176:179], v[98:101], 0
	v_and_b32_e32 v172, v175, v1
	v_and_b32_e32 v173, v175, v150
	v_and_b32_e32 v174, v175, v151
	v_and_b32_e32 v175, v175, v152
	ds_read_b128 v[176:179], v163 offset:1040
	v_mfma_i32_16x16x64_i8 v[74:77], v[180:183], v[74:77], 0
	s_waitcnt vmcnt(28)
	v_mfma_i32_16x16x64_i8 v[38:41], v[172:175], v[38:41], 0
	s_waitcnt lgkmcnt(0)
	v_and_b32_e32 v172, v176, v1
	v_and_b32_e32 v173, v176, v150
	v_and_b32_e32 v174, v176, v151
	v_and_b32_e32 v175, v176, v152
	s_waitcnt vmcnt(27)
	s_nop 0
	v_mfma_i32_16x16x64_i8 v[50:53], v[172:175], v[50:53], v[82:85]
	v_mov_b32_e32 v173, s11
	s_nop 1
	v_and_b32_e32 v82, v177, v1
	v_and_b32_e32 v83, v177, v150
	v_and_b32_e32 v84, v177, v151
	v_and_b32_e32 v85, v177, v152
	s_waitcnt vmcnt(26)
	s_nop 0
	v_mfma_i32_16x16x64_i8 v[34:37], v[82:85], v[34:37], v[74:77]
	ds_read_b128 v[82:85], v163 offset:1056
	s_nop 1
	v_and_b32_e32 v74, v178, v1
	v_and_b32_e32 v75, v178, v150
	v_and_b32_e32 v76, v178, v151
	v_and_b32_e32 v77, v178, v152
	s_waitcnt vmcnt(25)
	s_nop 0
	v_mfma_i32_16x16x64_i8 v[54:57], v[74:77], v[54:57], v[98:101]
	v_and_b32_e32 v74, v179, v1
	v_and_b32_e32 v75, v179, v150
	v_and_b32_e32 v76, v179, v151
	v_and_b32_e32 v77, v179, v152
	s_waitcnt vmcnt(24)
	s_nop 0
	v_mfma_i32_16x16x64_i8 v[26:29], v[74:77], v[26:29], v[38:41]
	s_waitcnt lgkmcnt(0)
	s_nop 1
	v_and_b32_e32 v38, v82, v1
	v_and_b32_e32 v39, v82, v150
	v_and_b32_e32 v40, v82, v151
	v_and_b32_e32 v41, v82, v152
	s_waitcnt vmcnt(23)
	s_nop 0
	v_mfma_i32_16x16x64_i8 v[38:41], v[38:41], v[46:49], v[50:53]
	v_and_b32_e32 v46, v83, v1
	v_and_b32_e32 v47, v83, v150
	v_and_b32_e32 v48, v83, v151
	v_and_b32_e32 v49, v83, v152
	v_and_b32_e32 v50, v84, v1
	v_and_b32_e32 v51, v84, v150
	v_and_b32_e32 v52, v84, v151
	v_and_b32_e32 v53, v84, v152
	s_waitcnt vmcnt(22)
	v_mfma_i32_16x16x64_i8 v[30:33], v[46:49], v[30:33], v[34:37]
	v_and_b32_e32 v46, v85, v1
	v_and_b32_e32 v47, v85, v150
	v_and_b32_e32 v48, v85, v151
	ds_read_b128 v[34:37], v163 offset:1072
	v_and_b32_e32 v49, v85, v152
	s_waitcnt vmcnt(21)
	v_mfma_i32_16x16x64_i8 v[22:25], v[50:53], v[22:25], v[54:57]
	s_waitcnt lgkmcnt(0)
	v_and_b32_e32 v50, v34, v1
	v_and_b32_e32 v51, v34, v150
	v_and_b32_e32 v52, v34, v151
	v_and_b32_e32 v53, v34, v152
	s_waitcnt vmcnt(20)
	v_mfma_i32_16x16x64_i8 v[14:17], v[46:49], v[14:17], v[26:29]
	s_nop 2
	v_and_b32_e32 v26, v36, v1
	v_and_b32_e32 v27, v36, v150
	v_and_b32_e32 v28, v36, v151
	v_and_b32_e32 v29, v36, v152
	s_waitcnt vmcnt(19)
	v_mfma_i32_16x16x64_i8 v[174:177], v[50:53], v[18:21], v[38:41]
	v_and_b32_e32 v18, v35, v1
	v_and_b32_e32 v19, v35, v150
	v_and_b32_e32 v20, v35, v151
	v_and_b32_e32 v21, v35, v152
	s_waitcnt vmcnt(17)
; #define LAS __attribute__((address_space(3)))
; __device__ __forceinline__ void acc_half_sel(i32x4 (&av)[4], const u32x4 (&R)[16], const LAS unsigned* cr  , int r, const unsigned (&mk)[4]) {
;     u32x4 c4[4];
; #pragma unroll
;     for (int q = 0; q < 4; ++q) c4[q] = *(const LAS u32x4*)(cr + r * 16 + 4 * q);
; #pragma unroll
;     for (int it = 0; it < 16; ++it) {
;         const unsigned rep = (it & 3) == 0 ? c4[it >> 2].x : (it & 3) == 1 ? c4[it >> 2].y : (it & 3) == 2 ? c4[it >> 2].z : c4[it >> 2].w;
;         i32x4 Aop; Aop.x = (int)(rep & mk[0]); Aop.y = (int)(rep & mk[1]); Aop.z = (int)(rep & mk[2]); Aop.w = (int)(rep & mk[3]);
;         av[it & 3] = __builtin_amdgcn_mfma_i32_16x16x64_i8(Aop, __builtin_bit_cast(i32x4, R[it]), av[it & 3], 0, 0, 0);
;     }
; }
	v_mfma_i32_16x16x64_i8 v[182:185], v[26:29], v[6:9], v[22:25]
	v_and_b32_e32 v6, v37, v1
	v_and_b32_e32 v7, v37, v150
	v_and_b32_e32 v8, v37, v151
	v_and_b32_e32 v9, v37, v152
	v_mfma_i32_16x16x64_i8 v[178:181], v[18:21], v[10:13], v[30:33]
	v_lshl_add_u64 v[10:11], v[142:143], 0, s[6:7]
	v_lshl_add_u64 v[12:13], v[144:145], 0, s[6:7]
	global_load_dword v171, v[10:11], off
	global_load_dword v172, v[10:11], off offset:256
	global_load_dword v166, v[12:13], off
	global_load_dword v165, v[12:13], off offset:256
	s_waitcnt vmcnt(20)
	v_mfma_i32_16x16x64_i8 v[186:189], v[6:9], v[2:5], v[14:17]
	ds_read2_b32 v[2:3], v164 offset0:128 offset1:132
	ds_read2_b32 v[4:5], v164 offset0:136 offset1:140
	s_lshl_b64 s[6:7], s[40:41], 12
	s_waitcnt lgkmcnt(1)
	v_add_u32_e32 v2, v2, v153
	v_add_u32_e32 v3, v3, v153
	global_load_dwordx4 v[98:101], v2, s[38:39]
	global_load_dwordx4 v[74:77], v3, s[38:39]
	s_waitcnt lgkmcnt(0)
	v_add_u32_e32 v4, v4, v153
	ds_read2_b32 v[2:3], v164 offset0:144 offset1:148
	v_add_u32_e32 v5, v5, v153
	global_load_dwordx4 v[82:85], v4, s[38:39]
	global_load_dwordx4 v[54:57], v5, s[38:39]
	ds_read2_b32 v[4:5], v164 offset0:152 offset1:156
	s_waitcnt lgkmcnt(1)
	v_add_u32_e32 v2, v2, v153
	v_add_u32_e32 v3, v3, v153
	global_load_dwordx4 v[50:53], v2, s[38:39]
	global_load_dwordx4 v[38:41], v3, s[38:39]
	s_waitcnt lgkmcnt(0)
	v_add_u32_e32 v4, v4, v153
	ds_read2_b32 v[2:3], v164 offset0:160 offset1:164
	v_add_u32_e32 v5, v5, v153
	global_load_dwordx4 v[46:49], v4, s[38:39]
	global_load_dwordx4 v[30:33], v5, s[38:39]
	ds_read2_b32 v[4:5], v164 offset0:168 offset1:172
	s_waitcnt lgkmcnt(1)
	v_add_u32_e32 v2, v2, v153
	v_add_u32_e32 v3, v3, v153
	global_load_dwordx4 v[34:37], v2, s[38:39]
	global_load_dwordx4 v[26:29], v3, s[38:39]
	s_waitcnt lgkmcnt(0)
	v_add_u32_e32 v4, v4, v153
	ds_read2_b32 v[2:3], v164 offset0:176 offset1:180
	v_add_u32_e32 v5, v5, v153
	global_load_dwordx4 v[22:25], v4, s[38:39]
	global_load_dwordx4 v[14:17], v5, s[38:39]
	ds_read2_b32 v[4:5], v164 offset0:184 offset1:188
	s_waitcnt lgkmcnt(1)
	v_add_u32_e32 v2, v2, v153
	v_add_u32_e32 v3, v3, v153
	global_load_dwordx4 v[18:21], v2, s[38:39]
	global_load_dwordx4 v[10:13], v3, s[38:39]
	s_waitcnt lgkmcnt(0)
	v_add_u32_e32 v2, v4, v153
	v_add_u32_e32 v3, v5, v153
	global_load_dwordx4 v[6:9], v2, s[38:39]
	s_nop 0
	global_load_dwordx4 v[2:5], v3, s[38:39]
	ds_read_b128 v[190:193], v163 offset:1280
	s_waitcnt lgkmcnt(0)
	v_and_b32_e32 v194, v190, v1
	v_and_b32_e32 v195, v190, v150
	v_and_b32_e32 v196, v190, v151
	v_and_b32_e32 v197, v190, v152
	s_waitcnt vmcnt(35)
	s_nop 0
	v_mfma_i32_16x16x64_i8 v[122:125], v[194:197], v[122:125], v[174:177]
	s_nop 2
	v_and_b32_e32 v174, v191, v1
	v_and_b32_e32 v175, v191, v150
	v_and_b32_e32 v176, v191, v151
	v_and_b32_e32 v177, v191, v152
	s_waitcnt vmcnt(34)
	s_nop 0
	v_mfma_i32_16x16x64_i8 v[118:121], v[174:177], v[118:121], v[178:181]
	v_and_b32_e32 v174, v192, v1
	v_and_b32_e32 v175, v192, v150
	v_and_b32_e32 v176, v192, v151
	v_and_b32_e32 v177, v192, v152
	ds_read_b128 v[178:181], v163 offset:1296
	s_waitcnt vmcnt(33)
	v_mfma_i32_16x16x64_i8 v[126:129], v[174:177], v[126:129], v[182:185]
	v_and_b32_e32 v174, v193, v1
	v_and_b32_e32 v175, v193, v150
	v_and_b32_e32 v176, v193, v151
	v_and_b32_e32 v177, v193, v152
	s_waitcnt vmcnt(32)
	s_nop 0
	v_mfma_i32_16x16x64_i8 v[90:93], v[174:177], v[90:93], v[186:189]
	s_waitcnt lgkmcnt(0)
	v_and_b32_e32 v174, v178, v1
	v_and_b32_e32 v175, v178, v150
	v_and_b32_e32 v176, v178, v151
	v_and_b32_e32 v177, v178, v152
	s_waitcnt vmcnt(31)
	s_nop 0
	v_mfma_i32_16x16x64_i8 v[106:109], v[174:177], v[106:109], v[122:125]
	s_nop 2
	v_and_b32_e32 v122, v179, v1
	v_and_b32_e32 v123, v179, v150
	v_and_b32_e32 v124, v179, v151
	v_and_b32_e32 v125, v179, v152
	s_waitcnt vmcnt(30)
	s_nop 0
	v_mfma_i32_16x16x64_i8 v[86:89], v[122:125], v[86:89], v[118:121]
	ds_read_b128 v[122:125], v163 offset:1312
	s_nop 1
	v_and_b32_e32 v118, v180, v1
	v_and_b32_e32 v119, v180, v150
	v_and_b32_e32 v120, v180, v151
	v_and_b32_e32 v121, v180, v152
	s_waitcnt vmcnt(29)
	s_nop 0
	v_mfma_i32_16x16x64_i8 v[110:113], v[118:121], v[110:113], v[126:129]
	v_and_b32_e32 v118, v181, v1
	v_and_b32_e32 v119, v181, v150
	v_and_b32_e32 v120, v181, v151
	v_and_b32_e32 v121, v181, v152
	s_waitcnt vmcnt(28)
	s_nop 0
	v_mfma_i32_16x16x64_i8 v[78:81], v[118:121], v[78:81], v[90:93]
	s_waitcnt lgkmcnt(0)
	s_nop 1
	v_and_b32_e32 v90, v122, v1
	v_and_b32_e32 v91, v122, v150
	v_and_b32_e32 v92, v122, v151
	v_and_b32_e32 v93, v122, v152
	s_waitcnt vmcnt(27)
	s_nop 0
	v_mfma_i32_16x16x64_i8 v[90:93], v[90:93], v[102:105], v[106:109]
	v_and_b32_e32 v102, v123, v1
	v_and_b32_e32 v103, v123, v150
	v_and_b32_e32 v104, v123, v151
	v_and_b32_e32 v105, v123, v152
	ds_read_b128 v[106:109], v163 offset:1328
	s_waitcnt vmcnt(26)
; #define LAS __attribute__((address_space(3)))
; __device__ __forceinline__ void peer_stage_lists(const PeerMeta& m, LAS int* es, LAS unsigned* crep, LAS float* scp, int lane) {
;     es[lane] = m.e[0] << 8; es[64 + lane] = m.e[1] << 8;
;     const float cmax = wave_max(fmaxf(fabsf(m.c[0]), fabsf(m.c[1])));
;     const float inv = cmax > 0.f ? 127.0f / cmax : 0.f;
;     if (lane == 0) scp[0] = cmax * (1.0f / 127.0f);
	v_mfma_i32_16x16x64_i8 v[86:89], v[102:105], v[94:97], v[86:89]
	v_and_b32_e32 v102, v125, v1
	v_and_b32_e32 v103, v125, v150
	v_and_b32_e32 v104, v125, v151
	v_and_b32_e32 v105, v125, v152
	v_and_b32_e32 v94, v124, v1
	v_and_b32_e32 v95, v124, v150
	s_waitcnt vmcnt(24)
	v_mfma_i32_16x16x64_i8 v[66:69], v[102:105], v[66:69], v[78:81]
	v_and_b32_e32 v96, v124, v151
	s_waitcnt lgkmcnt(0)
	s_nop 0
	v_and_b32_e32 v78, v106, v1
	v_and_b32_e32 v79, v106, v150
	v_and_b32_e32 v80, v106, v151
	v_and_b32_e32 v81, v106, v152
	v_and_b32_e32 v97, v124, v152
	s_waitcnt vmcnt(23)
	v_mfma_i32_16x16x64_i8 v[174:177], v[78:81], v[70:73], v[90:93]
	v_and_b32_e32 v70, v107, v1
	v_and_b32_e32 v71, v107, v150
	v_and_b32_e32 v72, v107, v151
	v_and_b32_e32 v73, v107, v152
	v_mfma_i32_16x16x64_i8 v[94:97], v[94:97], v[114:117], v[110:113]
	s_waitcnt vmcnt(22)
	v_mfma_i32_16x16x64_i8 v[178:181], v[70:73], v[62:65], v[86:89]
	v_and_b32_e32 v62, v108, v1
	v_and_b32_e32 v63, v108, v150
	v_and_b32_e32 v64, v108, v151
	v_and_b32_e32 v65, v108, v152
	s_waitcnt vmcnt(21)
	s_nop 0
	v_mfma_i32_16x16x64_i8 v[182:185], v[62:65], v[58:61], v[94:97]
	v_and_b32_e32 v58, v109, v1
	v_and_b32_e32 v59, v109, v150
	v_and_b32_e32 v60, v109, v151
	v_and_b32_e32 v61, v109, v152
	s_waitcnt vmcnt(20)
	s_nop 0
	v_mfma_i32_16x16x64_i8 v[186:189], v[58:61], v[42:45], v[66:69]
	ds_read2_b32 v[42:43], v164 offset0:192 offset1:196
	ds_read2_b32 v[44:45], v164 offset0:200 offset1:204
	v_add_u32_e32 v176, v176, v180
	v_add_u32_e32 v174, v174, v178
	s_nop 3
	v_add3_u32 v178, v176, v188, v184
	s_waitcnt lgkmcnt(1)
	v_add_u32_e32 v42, v42, v153
	v_add_u32_e32 v43, v43, v153
	global_load_dwordx4 v[126:129], v42, s[38:39]
	global_load_dwordx4 v[118:121], v43, s[38:39]
	s_waitcnt lgkmcnt(0)
	v_add_u32_e32 v44, v44, v153
	ds_read2_b32 v[42:43], v164 offset0:208 offset1:212
	v_add_u32_e32 v45, v45, v153
	global_load_dwordx4 v[122:125], v44, s[38:39]
	global_load_dwordx4 v[114:117], v45, s[38:39]
	ds_read2_b32 v[44:45], v164 offset0:216 offset1:220
	v_add3_u32 v180, v174, v186, v182
	s_waitcnt lgkmcnt(1)
	v_add_u32_e32 v42, v42, v153
	v_add_u32_e32 v43, v43, v153
	global_load_dwordx4 v[110:113], v42, s[38:39]
	global_load_dwordx4 v[102:105], v43, s[38:39]
	s_waitcnt lgkmcnt(0)
	v_add_u32_e32 v44, v44, v153
	ds_read2_b32 v[42:43], v164 offset0:224 offset1:228
	v_add_u32_e32 v45, v45, v153
	global_load_dwordx4 v[106:109], v44, s[38:39]
	global_load_dwordx4 v[86:89], v45, s[38:39]
	ds_read2_b32 v[44:45], v164 offset0:232 offset1:236
	v_add_u32_e32 v177, v177, v181
	s_waitcnt lgkmcnt(1)
	v_add_u32_e32 v42, v42, v153
	v_add_u32_e32 v43, v43, v153
	global_load_dwordx4 v[94:97], v42, s[38:39]
	global_load_dwordx4 v[78:81], v43, s[38:39]
	s_waitcnt lgkmcnt(0)
	v_add_u32_e32 v44, v44, v153
	ds_read2_b32 v[42:43], v164 offset0:240 offset1:244
	v_add_u32_e32 v45, v45, v153
	global_load_dwordx4 v[90:93], v44, s[38:39]
	global_load_dwordx4 v[70:73], v45, s[38:39]
	ds_read2_b32 v[44:45], v164 offset0:248 offset1:252
	v_cvt_f32_i32_e32 v178, v178
	s_waitcnt lgkmcnt(1)
	v_add_u32_e32 v42, v42, v153
	v_add_u32_e32 v43, v43, v153
	global_load_dwordx4 v[66:69], v42, s[38:39]
	global_load_dwordx4 v[62:65], v43, s[38:39]
	s_waitcnt lgkmcnt(0)
	v_add_u32_e32 v42, v44, v153
	v_add_u32_e32 v43, v45, v153
	global_load_dwordx4 v[58:61], v42, s[38:39]
	s_nop 0
	global_load_dwordx4 v[42:45], v43, s[38:39]
	ds_read_b32 v190, v173 offset:2048
	v_add_u32_e32 v173, v175, v179
	v_max_f32_e64 v175, |v167|, |v167|
	v_max_f32_e64 v179, |v168|, |v168|
	v_max_f32_e32 v175, v179, v175
	ds_bpermute_b32 v179, v155, v175
	v_add3_u32 v173, v173, v187, v183
	s_waitcnt lgkmcnt(0)
	v_max_f32_e32 v176, v179, v179
	v_max_f32_e32 v175, v175, v176
	ds_bpermute_b32 v176, v156, v175
	v_add3_u32 v179, v177, v189, v185
	v_cvt_f32_i32_e32 v177, v173
	v_cvt_f32_i32_e32 v179, v179
	s_waitcnt lgkmcnt(0)
	v_max_f32_e32 v174, v176, v176
	v_max_f32_e32 v181, v175, v174
	ds_bpermute_b32 v182, v157, v181
	v_cvt_f32_i32_e32 v176, v180
	v_pk_mul_f32 v[178:179], v[190:191], v[178:179] op_sel_hi:[0,1]
	v_lshl_add_u64 v[174:175], v[148:149], 0, s[6:7]
	s_waitcnt lgkmcnt(0)
	v_max_f32_e32 v173, v182, v182
	v_max_f32_e32 v173, v181, v173
	ds_bpermute_b32 v180, v158, v173
	v_pk_mul_f32 v[176:177], v[190:191], v[176:177] op_sel_hi:[0,1]
	v_cvt_pk_bf16_f32 v176, v176, v177
	s_waitcnt lgkmcnt(0)
	v_max_f32_e32 v177, v180, v180
	v_max_f32_e32 v173, v173, v177
	ds_bpermute_b32 v180, v159, v173
	v_cvt_pk_bf16_f32 v177, v178, v179
	global_store_dwordx2 v[174:175], v[176:177], off
	s_waitcnt vmcnt(37)
	s_waitcnt lgkmcnt(0)
	v_max_f32_e32 v174, v180, v180
	v_max_f32_e32 v173, v173, v174
	ds_bpermute_b32 v174, v160, v173
	ds_write2st64_b32 v154, v169, v170 offset1:1
	s_waitcnt lgkmcnt(1)
	v_max_f32_e32 v169, v174, v174
	v_max_f32_e32 v169, v173, v169
	s_and_saveexec_b64 s[6:7], s[2:3]
	s_cbranch_execz .LBB0_945
	v_mul_f32_e32 v170, 0x3c010204, v169
	v_mov_b32_e32 v173, s11
	ds_write_b32 v173, v170 offset:2048
	s_branch .LBB0_945
